# hgrn_prep item loop: counted vmcnt waits (loop top no longer drains the previous item's stores; the lower-bound load no longer waits for the next item's operand prefetch)
# speedup vs baseline: 1.0076x; 1.0068x over previous
.LBB0_3010:
	s_cmp_gt_i32 s6, 51
	s_cselect_b64 s[0:1], -1, 0
	s_cmp_lt_i32 s7, 52
	s_cselect_b64 s[2:3], -1, 0
	s_or_b64 s[0:1], s[0:1], s[2:3]
	s_and_b64 vcc, exec, s[0:1]
	s_cbranch_vccnz .LBB0_3080
	s_cmpk_gt_i32 s88, 0xfff
	s_waitcnt vmcnt(0)
	v_mbcnt_lo_u32_b32 v17, -1, 0
	v_mbcnt_hi_u32_b32 v17, -1, v17
	s_cbranch_scc1 .LBB0_3030
	s_add_u32 s44, s94, 0x400000
	v_readlane_b32 s9, v253, 20
	s_addc_u32 s45, s95, 0
	s_and_b32 s0, s89, 0xffffffc0
	s_lshl_b32 s6, s9, 3
	v_add_u32_e32 v26, s0, v17
	s_add_u32 s0, s94, 0x3d600000
	s_addc_u32 s1, s95, 0
	s_lshl_b32 s3, s88, 6
	s_bfe_u32 s7, s88, 0x10006
	s_and_b32 s4, s88, 0x380
	s_ashr_i32 s2, s88, 10
	s_and_b32 s8, s3, 0xfc0
	s_cmp_eq_u32 s7, 0
	v_ashrrev_i32_e32 v70, 4, v26
	v_add_u32_e32 v2, s8, v70
	s_cselect_b64 vcc, -1, 0
	s_ashr_i32 s3, s2, 31
	v_sub_u32_e32 v3, 0xfff, v2
	s_lshl_b64 s[2:3], s[2:3], 12
	s_lshl_b32 s4, s4, 1
	s_add_u32 s4, s0, s4
	v_lshlrev_b32_e32 v0, 4, v17
	v_cndmask_b32_e32 v2, v3, v2, vcc
	s_addc_u32 s5, s1, 0
	v_and_b32_e32 v18, 0xf0, v0
	v_mov_b32_e32 v19, 0
	v_ashrrev_i32_e32 v3, 31, v2
	v_lshl_add_u64 v[0:1], s[4:5], 0, v[18:19]
	v_lshl_add_u64 v[2:3], s[2:3], 0, v[2:3]
	s_movk_i32 s33, 0x2800
	v_mad_u64_u32 v[8:9], s[4:5], v2, s33, v[0:1]
	v_add_u32_e32 v2, 0x200, v26
	v_ashrrev_i32_e32 v71, 4, v2
	v_add_u32_e32 v2, s8, v71
	v_mad_i32_i24 v9, v3, s33, v9
	v_sub_u32_e32 v3, 0xfff, v2
	v_cndmask_b32_e32 v2, v3, v2, vcc
	v_ashrrev_i32_e32 v3, 31, v2
	v_lshl_add_u64 v[2:3], s[2:3], 0, v[2:3]
	s_mov_b32 s47, 0
	s_lshl_b32 s46, s7, 11
	v_mad_u64_u32 v[10:11], s[2:3], v2, s33, v[0:1]
	v_lshl_add_u64 v[20:21], v[8:9], 0, s[46:47]
	v_mad_i32_i24 v11, v3, s33, v11
	global_load_dwordx4 v[0:3], v[8:9], off
	global_load_dwordx4 v[4:7], v[10:11], off
	v_lshl_add_u64 v[22:23], v[10:11], 0, s[46:47]
	global_load_dwordx4 v[8:11], v[20:21], off offset:2048
	global_load_dwordx4 v[12:15], v[22:23], off offset:2048
	v_lshl_add_u64 v[18:19], s[0:1], 0, v[18:19]
	s_lshl_b32 s0, s9, 9
	s_add_i32 s56, s0, 0
	s_movk_i32 s42, 0x120
	s_add_i32 s0, 0, 0x11800
	s_lshl_b32 s46, s9, 4
	v_mul_lo_u32 v20, v17, s42
	s_cmp_lt_u32 s89, 64
	v_add_u32_e32 v40, s0, v20
	s_cselect_b64 s[48:49], -1, 0
	s_lshl_b32 s0, s9, 5
	v_and_b32_e32 v24, 15, v17
	s_and_b32 s22, s0, 32
	s_and_b32 s0, s6, 0x1ffffff0
	v_or_b32_e32 v20, s0, v24
	s_movk_i32 s23, 0x110
	v_mul_lo_u32 v21, v20, s23
	s_movk_i32 s0, 0x90
	s_lshl_b32 s57, s9, 11
	s_or_b32 s65, s6, 7
	v_add_u32_e32 v42, 0, v21
	v_mul_lo_u32 v21, v20, s0
	s_add_i32 s0, 0, 0x16000
	s_or_b32 s58, s57, 0x100
	s_or_b32 s59, s57, 0x200
	s_or_b32 s60, s57, 0x300
	s_or_b32 s61, s57, 0x400
	s_or_b32 s62, s57, 0x500
	s_or_b32 s63, s57, 0x600
	s_lshl_b32 s64, s65, 8
	s_cmpk_gt_u32 s89, 0x7f
	v_add_u32_e32 v43, s0, v21
	s_cselect_b64 s[0:1], -1, 0
	s_cmpk_gt_u32 s89, 0xbf
	s_cselect_b64 s[2:3], -1, 0
	s_cmpk_gt_u32 s89, 0xff
	s_cselect_b64 s[4:5], -1, 0
	s_cmpk_gt_u32 s89, 0x13f
	v_lshlrev_b32_e32 v68, 1, v17
	v_lshlrev_b32_e32 v69, 3, v17
	v_lshl_add_u32 v72, v17, 2, 0
	v_and_b32_e32 v41, -16, v17
	v_ashrrev_i32_e32 v17, 2, v17
	s_cselect_b64 s[6:7], -1, 0
	s_cmpk_gt_u32 s89, 0x17f
	v_and_b32_e32 v17, -4, v17
	s_cselect_b64 s[8:9], -1, 0
	s_cmpk_gt_u32 s89, 0x1bf
	v_or_b32_e32 v21, s22, v24
	s_cselect_b64 s[10:11], -1, 0
	s_cmpk_gt_u32 s89, 0x1ff
	v_mad_u32_u24 v44, v21, s23, 0
	v_add_u32_e32 v21, s22, v17
	s_cselect_b64 s[12:13], -1, 0
	v_or_b32_e32 v22, 2, v21
	s_or_b32 s22, s22, 16
	v_cmp_gt_i32_e64 s[14:15], v21, v20
	v_cmp_lt_i32_e64 s[16:17], v21, v20
	v_cmp_gt_i32_e64 s[18:19], v22, v20
	v_or_b32_e32 v22, 3, v21
	v_lshlrev_b32_e32 v45, 1, v21
	v_or_b32_e32 v21, s22, v24
	v_add_u32_e32 v17, s22, v17
	v_mad_u32_u24 v46, v21, s23, 0
	v_or_b32_e32 v21, 2, v17
	v_lshlrev_b32_e32 v16, 4, v26
	v_cmp_gt_i32_e64 s[26:27], v21, v20
	v_or_b32_e32 v21, 3, v17
	s_movk_i32 s30, 0xb20
	s_movk_i32 s34, 0x920
	s_movk_i32 s36, 0x720
	s_movk_i32 s38, 0x520
	s_movk_i32 s40, 0x320
	v_add_u32_e32 v30, 0x2000, v16
	v_cmp_gt_i32_e64 s[20:21], v22, v20
	v_cmp_gt_i32_e64 s[22:23], v17, v20
	v_cmp_lt_i32_e64 s[24:25], v17, v20
	v_cmp_gt_i32_e64 s[28:29], v21, v20
	v_cmp_gt_i32_e64 s[30:31], s30, v26
	v_cmp_gt_i32_e64 s[34:35], s34, v26
	v_cmp_gt_i32_e64 s[36:37], s36, v26
	v_add_u32_e32 v20, 0x4000, v16
	v_cmp_gt_i32_e64 s[38:39], s38, v26
	v_add_u32_e32 v22, 0x6000, v16
	v_cmp_gt_i32_e64 s[40:41], s40, v26
	v_add_u32_e32 v24, 0x8000, v16
	v_cmp_gt_i32_e64 s[42:43], s42, v26
	v_add_u32_e32 v26, 0xa000, v16
	s_mul_i32 s50, s88, 0xb200
	v_lshlrev_b32_e32 v47, 1, v17
	v_ashrrev_i32_e32 v17, 31, v16
	v_ashrrev_i32_e32 v31, 31, v30
	v_ashrrev_i32_e32 v21, 31, v20
	v_ashrrev_i32_e32 v23, 31, v22
	v_ashrrev_i32_e32 v25, 31, v24
	v_ashrrev_i32_e32 v27, 31, v26
	s_mov_b64 s[52:53], 0x17600000
	s_mul_hi_i32 s51, s88, 0xb200
	s_add_u32 s50, s94, s50
	v_lshl_add_u64 v[28:29], v[16:17], 0, s[52:53]
	s_addc_u32 s51, s95, s51
	v_lshl_add_u64 v[30:31], v[30:31], 0, s[52:53]
	v_lshl_add_u64 v[32:33], v[20:21], 0, s[52:53]
	v_lshl_add_u64 v[34:35], v[22:23], 0, s[52:53]
	v_lshl_add_u64 v[36:37], v[24:25], 0, s[52:53]
	v_lshl_add_u64 v[38:39], v[26:27], 0, s[52:53]
	s_add_i32 s52, s90, s88
	s_mulk_i32 s65, 0x110
	s_lshl_b32 s66, s52, 6
	s_lshl_b32 s67, s90, 6
	v_add_u32_e32 v17, s46, v40
	v_add_u32_e32 v21, v44, v41
	v_add_u32_e32 v23, v42, v41
	v_add_u32_e32 v25, v43, v45
	v_add_u32_e32 v27, v46, v41
	v_add_u32_e32 v73, v43, v47
	s_mov_b32 s68, s88
	s_waitcnt vmcnt(0)
	s_branch .LBB0_3014
.Lhp_last:
	s_waitcnt vmcnt(0)
	s_branch .LBB0_3016

.LBB0_3014:
	s_and_b32 s46, s68, 0x380
	v_add_u32_e32 v40, s46, v68
	v_ashrrev_i32_e32 v41, 31, v40
	v_lshl_add_u64 v[40:41], v[40:41], 2, s[44:45]
	global_load_dwordx2 v[54:55], v[40:41], off
	s_add_i32 s68, s68, s90
	s_cmpk_gt_i32 s68, 0xfff
	s_cselect_b64 s[52:53], -1, 0
	v_add_u32_e32 v74, 0, v16
	s_and_b64 vcc, exec, s[52:53]
	s_waitcnt vmcnt(6)
	ds_write_b128 v74, v[0:3]
	s_waitcnt vmcnt(6)
	ds_write_b128 v74, v[8:11] offset:16384
	ds_write_b128 v74, v[4:7] offset:8192
	s_waitcnt vmcnt(6)
	ds_write_b128 v74, v[12:15] offset:24576
	s_cbranch_vccnz .Lhp_last
	s_bfe_u32 s69, s68, 0x10006
	s_and_b32 s46, s68, 0x380
	s_ashr_i32 s54, s68, 10
	s_and_b32 s72, s66, 0xfc0
	s_cmp_eq_u32 s69, 0
	v_add_u32_e32 v2, s72, v70
	v_sub_u32_e32 v3, 0xfff, v2
	s_cselect_b64 vcc, -1, 0
	s_ashr_i32 s55, s54, 31
	v_cndmask_b32_e32 v2, v3, v2, vcc
	s_lshl_b64 s[54:55], s[54:55], 12
	s_lshl_b32 s46, s46, 1
	v_ashrrev_i32_e32 v3, 31, v2
	v_lshl_add_u64 v[0:1], v[18:19], 0, s[46:47]
	v_lshl_add_u64 v[2:3], s[54:55], 0, v[2:3]
	v_mad_u64_u32 v[4:5], s[70:71], v2, s33, v[0:1]
	v_add_u32_e32 v2, s72, v71
	v_mad_i32_i24 v5, v3, s33, v5
	v_sub_u32_e32 v3, 0xfff, v2
	v_cndmask_b32_e32 v2, v3, v2, vcc
	v_ashrrev_i32_e32 v3, 31, v2
	v_lshl_add_u64 v[2:3], s[54:55], 0, v[2:3]
	v_mad_u64_u32 v[10:11], s[54:55], v2, s33, v[0:1]
	s_lshl_b32 s46, s69, 11
	v_mad_i32_i24 v11, v3, s33, v11
	v_lshl_add_u64 v[8:9], v[4:5], 0, s[46:47]
	v_lshl_add_u64 v[12:13], v[10:11], 0, s[46:47]
	global_load_dwordx4 v[0:3], v[4:5], off
	s_nop 0
	global_load_dwordx4 v[4:7], v[10:11], off
	s_nop 0
	global_load_dwordx4 v[8:11], v[8:9], off offset:2048
	s_nop 0
	global_load_dwordx4 v[12:15], v[12:13], off offset:2048
.LBB0_3016:
	v_add_u32_e32 v75, s57, v72
	s_waitcnt lgkmcnt(0)
	s_barrier
	v_add_u32_e32 v76, s58, v72
	v_add_u32_e32 v77, s59, v72
	v_add_u32_e32 v106, s60, v72
	v_add_u32_e32 v107, s61, v72
	v_add_u32_e32 v108, s62, v72
	v_add_u32_e32 v102, s63, v72
	v_add_u32_e32 v104, s64, v72
	ds_read_b32 v40, v75 offset:16384
	ds_read_b32 v43, v76 offset:16384
	ds_read_b32 v46, v77 offset:16384
	ds_read_b32 v47, v106 offset:16384
	ds_read_b32 v48, v107 offset:16384
	ds_read_b32 v49, v108 offset:16384
	ds_read_b32 v50, v102 offset:16384
	ds_read_b32 v51, v104 offset:16384
	s_waitcnt lgkmcnt(7)
	v_lshlrev_b32_e32 v41, 16, v40
	v_and_b32_e32 v40, 0xffff0000, v40
	v_mul_f32_e32 v40, 0xbfb8aa3b, v40
	s_waitcnt lgkmcnt(6)
	v_lshlrev_b32_e32 v45, 16, v43
	v_exp_f32_e32 v44, v40
	v_mul_f32_e32 v45, 0xbfb8aa3b, v45
	v_exp_f32_e32 v52, v45
	s_waitcnt lgkmcnt(4)
	v_lshlrev_b32_e32 v53, 16, v47
	v_add_f32_e32 v44, 1.0, v44
	v_rcp_f32_e32 v45, v44
	v_add_f32_e32 v44, 1.0, v52
	v_lshlrev_b32_e32 v52, 16, v46
	v_and_b32_e32 v46, 0xffff0000, v46
	v_mul_f32_e32 v46, 0xbfb8aa3b, v46
	v_exp_f32_e32 v46, v46
	v_mul_f32_e32 v53, 0xbfb8aa3b, v53
	v_and_b32_e32 v47, 0xffff0000, v47
	v_exp_f32_e32 v56, v53
	v_mul_f32_e32 v47, 0xbfb8aa3b, v47
	v_exp_f32_e32 v47, v47
	v_add_f32_e32 v46, 1.0, v46
	v_rcp_f32_e32 v53, v46
	v_add_f32_e32 v46, 1.0, v56
	v_rcp_f32_e32 v62, v46
	v_add_f32_e32 v46, 1.0, v47
	s_waitcnt lgkmcnt(3)
	v_lshlrev_b32_e32 v47, 16, v48
	v_mul_f32_e32 v47, 0xbfb8aa3b, v47
	v_and_b32_e32 v48, 0xffff0000, v48
	v_exp_f32_e32 v47, v47
	v_mul_f32_e32 v48, 0xbfb8aa3b, v48
	v_exp_f32_e32 v48, v48
	v_rcp_f32_e32 v63, v46
	v_add_f32_e32 v46, 1.0, v47
	s_waitcnt lgkmcnt(2)
	v_lshlrev_b32_e32 v47, 16, v49
	v_rcp_f32_e32 v66, v46
	v_add_f32_e32 v46, 1.0, v48
	v_mul_f32_e32 v47, 0xbfb8aa3b, v47
	v_and_b32_e32 v48, 0xffff0000, v49
	v_exp_f32_e32 v47, v47
	v_mul_f32_e32 v48, 0xbfb8aa3b, v48
	v_exp_f32_e32 v48, v48
	v_rcp_f32_e32 v67, v46
	v_add_f32_e32 v46, 1.0, v47
	s_waitcnt lgkmcnt(1)
	v_lshlrev_b32_e32 v47, 16, v50
	v_rcp_f32_e32 v90, v46
	v_add_f32_e32 v46, 1.0, v48
	v_mul_f32_e32 v47, 0xbfb8aa3b, v47
	v_and_b32_e32 v48, 0xffff0000, v50
	v_exp_f32_e32 v47, v47
	v_mul_f32_e32 v48, 0xbfb8aa3b, v48
	v_and_b32_e32 v43, 0xffff0000, v43
	v_exp_f32_e32 v48, v48
	v_mul_f32_e32 v41, 0xbfb8aa3b, v41
	v_mul_f32_e32 v43, 0xbfb8aa3b, v43
	v_exp_f32_e32 v42, v41
	v_exp_f32_e32 v43, v43
	v_mul_f32_e32 v52, 0xbfb8aa3b, v52
	v_exp_f32_e32 v52, v52
	v_rcp_f32_e32 v91, v46
	v_add_f32_e32 v46, 1.0, v47
	s_waitcnt lgkmcnt(0)
	v_lshlrev_b32_e32 v47, 16, v51
	v_rcp_f32_e32 v92, v46
	v_add_f32_e32 v46, 1.0, v48
	v_mul_f32_e32 v47, 0xbfb8aa3b, v47
	v_and_b32_e32 v48, 0xffff0000, v51
	v_exp_f32_e32 v47, v47
	v_mul_f32_e32 v48, 0xbfb8aa3b, v48
	v_add_f32_e32 v42, 1.0, v42
	v_add_f32_e32 v43, 1.0, v43
	v_exp_f32_e32 v48, v48
	v_rcp_f32_e32 v42, v42
	v_rcp_f32_e32 v44, v44
	v_rcp_f32_e32 v43, v43
	v_add_f32_e32 v52, 1.0, v52
	v_rcp_f32_e32 v52, v52
	v_rcp_f32_e32 v93, v46
	v_add_f32_e32 v46, 1.0, v47
	s_waitcnt vmcnt(4)
	v_pk_add_f32 v[40:41], v[54:55], 1.0 op_sel_hi:[1,0] neg_lo:[1,0] neg_hi:[1,0]
	v_rcp_f32_e32 v60, v46
	v_add_f32_e32 v46, 1.0, v48
	v_rcp_f32_e32 v61, v46
	v_pk_fma_f32 v[46:47], v[40:41], v[44:45], v[54:55]
	v_pk_fma_f32 v[48:49], v[40:41], v[42:43], v[54:55]
	v_pk_fma_f32 v[56:57], v[40:41], v[52:53], v[54:55]
	v_pk_mul_f32 v[50:51], v[46:47], v[48:49]
	v_add_u32_e32 v46, s56, v69
	v_pk_mul_f32 v[58:59], v[50:51], v[56:57]
	v_pk_fma_f32 v[56:57], v[40:41], v[62:63], v[54:55]
	v_sub_f32_e32 v49, 1.0, v60
	v_pk_mul_f32 v[64:65], v[58:59], v[56:57]
	v_pk_fma_f32 v[56:57], v[40:41], v[66:67], v[54:55]
	v_mul_f32_e32 v103, v40, v49
	v_pk_mul_f32 v[94:95], v[64:65], v[56:57]
	v_pk_fma_f32 v[56:57], v[40:41], v[90:91], v[54:55]
	v_sub_f32_e32 v49, 1.0, v61
	v_pk_mul_f32 v[96:97], v[94:95], v[56:57]
	v_pk_fma_f32 v[56:57], v[40:41], v[92:93], v[54:55]
	v_pk_fma_f32 v[54:55], v[40:41], v[60:61], v[54:55]
	v_pk_mul_f32 v[98:99], v[96:97], v[56:57]
	v_mul_f32_e32 v105, v41, v49
	v_pk_mul_f32 v[100:101], v[98:99], v[54:55]
	ds_write_b64 v46, v[100:101] offset:50176
	v_add_u32_e32 v46, 0, v69
	s_waitcnt lgkmcnt(0)
	s_barrier
	ds_read2st64_b64 v[54:57], v46 offset0:98 offset1:99
	ds_read2st64_b64 v[78:81], v46 offset0:100 offset1:101
	v_readlane_b32 s46, v253, 20
	s_mulk_i32 s46, 0x880
	s_andn2_b64 vcc, exec, s[48:49]
	s_waitcnt lgkmcnt(1)
	v_cndmask_b32_e64 v49, v55, 1.0, s[48:49]
	v_mul_f32_e32 v82, v49, v57
	v_cndmask_b32_e64 v60, v54, 1.0, s[48:49]
	v_cndmask_b32_e64 v49, v49, v82, s[0:1]
	v_mul_f32_e32 v61, v60, v56
	s_waitcnt lgkmcnt(0)
	v_mul_f32_e32 v82, v79, v49
	v_cndmask_b32_e64 v60, v60, v61, s[0:1]
	v_cndmask_b32_e64 v49, v49, v82, s[2:3]
	ds_read2st64_b64 v[82:85], v46 offset0:102 offset1:103
	v_mul_f32_e32 v61, v78, v60
	v_cndmask_b32_e64 v60, v60, v61, s[2:3]
	v_mul_f32_e32 v61, v80, v60
	v_mul_f32_e32 v86, v81, v49
	v_cndmask_b32_e64 v49, v49, v86, s[4:5]
	v_cndmask_b32_e64 v60, v60, v61, s[4:5]
	ds_read2st64_b64 v[86:89], v46 offset0:104 offset1:105
	s_waitcnt lgkmcnt(1)
	v_mul_f32_e32 v61, v82, v60
	v_cndmask_b32_e64 v60, v60, v61, s[6:7]
	v_mul_f32_e32 v61, v84, v60
	v_cndmask_b32_e64 v60, v60, v61, s[8:9]
	s_waitcnt lgkmcnt(0)
	v_mul_f32_e32 v61, v86, v60
	v_mul_f32_e32 v109, v83, v49
	v_cndmask_b32_e64 v60, v60, v61, s[10:11]
	ds_read_b32 v61, v104
	v_cndmask_b32_e64 v49, v49, v109, s[6:7]
	v_mul_f32_e32 v109, v85, v49
	v_cndmask_b32_e64 v49, v49, v109, s[8:9]
	v_mul_f32_e32 v109, v87, v49
	v_pk_mul_f32 v[54:55], v[54:55], v[56:57]
	v_mul_f32_e32 v56, v88, v60
	v_cndmask_b32_e64 v49, v49, v109, s[10:11]
	v_cndmask_b32_e64 v109, v60, v56, s[12:13]
	s_waitcnt lgkmcnt(0)
	v_lshlrev_b32_e32 v60, 16, v61
	v_pk_mul_f32 v[54:55], v[54:55], v[78:79]
	v_and_b32_e32 v78, 0xffff0000, v61
	v_mul_f32_e32 v61, 0xbfb8aa3b, v60
	v_exp_f32_e32 v61, v61
	v_mul_f32_e32 v79, 0xbfb8aa3b, v78
	v_exp_f32_e32 v79, v79
	v_pk_mul_f32 v[54:55], v[54:55], v[80:81]
	v_add_f32_e32 v61, 1.0, v61
	v_mul_f32_e32 v57, v89, v49
	v_rcp_f32_e32 v81, v61
	v_add_f32_e32 v61, 1.0, v79
	v_cndmask_b32_e64 v49, v49, v57, s[12:13]
	v_rcp_f32_e32 v79, v61
	v_mul_f32_e32 v56, v100, v109
	v_mul_f32_e32 v80, v101, v49
	v_rcp_f32_e32 v57, v56
	v_rcp_f32_e32 v61, v80
	v_mul_f32_e32 v60, v81, v60
	v_mul_f32_e32 v56, v60, v56
	v_mul_f32_e32 v60, v79, v78
	v_mul_f32_e32 v60, v60, v80
	v_cvt_pk_bf16_f32 v56, v56, v60
	v_add_u32_e32 v100, s65, v72
	ds_write_b32 v100, v56 offset:54272
	v_mul_f32_e32 v56, v103, v57
	v_mul_f32_e32 v60, v105, v61
	v_cvt_pk_bf16_f32 v78, v56, v60
	ds_read_b32 v79, v102
	v_pk_mul_f32 v[54:55], v[54:55], v[82:83]
	v_mov_b32_e32 v102, v92
	v_pk_mul_f32 v[54:55], v[54:55], v[84:85]
	ds_write_b32 v100, v78 offset:32768
	v_pk_mul_f32 v[54:55], v[54:55], v[86:87]
	s_waitcnt lgkmcnt(1)
	v_lshlrev_b32_e32 v101, 16, v79
	v_pk_mul_f32 v[54:55], v[54:55], v[88:89]
	v_and_b32_e32 v110, 0xffff0000, v79
	v_mul_f32_e32 v88, v54, v56
	v_pk_add_f32 v[78:79], v[102:103], 1.0 op_sel_hi:[1,0] neg_lo:[1,0] neg_hi:[1,0]
	v_mov_b32_e32 v56, v40
	v_mov_b32_e32 v104, v93
	v_mul_f32_e32 v89, v55, v60
	v_pk_mul_f32 v[80:81], v[56:57], v[78:79]
	v_pk_add_f32 v[82:83], v[104:105], 1.0 op_sel_hi:[1,0] neg_lo:[1,0] neg_hi:[1,0]
	v_mov_b32_e32 v60, v41
	v_mul_f32_e32 v56, 0xbfb8aa3b, v101
	v_pk_mul_f32 v[84:85], v[60:61], v[82:83]
	v_exp_f32_e32 v56, v56
	v_mul_f32_e32 v60, 0xbfb8aa3b, v110
	v_exp_f32_e32 v60, v60
	v_mul_f32_e32 v98, v98, v109
	v_add_f32_e32 v56, 1.0, v56
	v_rcp_f32_e32 v56, v56
	v_add_f32_e32 v60, 1.0, v60
	v_rcp_f32_e32 v60, v60
	v_mul_f32_e32 v99, v99, v49
	v_mul_f32_e32 v56, v56, v101
	v_mov_b32_e32 v86, v90
	v_mov_b32_e32 v87, v80
	v_mul_f32_e32 v56, v98, v56
	v_mul_f32_e32 v60, v60, v110
	v_pk_add_f32 v[86:87], v[86:87], 1.0 op_sel_hi:[1,0] neg_lo:[1,0] neg_hi:[1,0]
	v_mov_b32_e32 v78, v40
	v_mul_f32_e32 v60, v99, v60
	v_cvt_pk_bf16_f32 v56, v56, v60
	v_pk_mul_f32 v[78:79], v[78:79], v[86:87]
	v_mov_b32_e32 v87, v84
	ds_write_b32 v100, v56 offset:54000
	v_mul_f32_e32 v56, v80, v81
	v_mul_f32_e32 v60, v84, v85
	v_cvt_pk_bf16_f32 v84, v56, v60
	ds_read_b32 v85, v108
	v_mov_b32_e32 v86, v91
	v_pk_add_f32 v[86:87], v[86:87], 1.0 op_sel_hi:[1,0] neg_lo:[1,0] neg_hi:[1,0]
	v_mov_b32_e32 v82, v41
	v_pk_mul_f32 v[80:81], v[82:83], v[86:87]
	s_waitcnt lgkmcnt(0)
	v_lshlrev_b32_e32 v86, 16, v85
	v_mov_b32_e32 v82, v66
	v_mov_b32_e32 v83, v78
	ds_write_b32 v100, v84 offset:32496
	v_and_b32_e32 v87, 0xffff0000, v85
	v_mul_f32_e32 v92, v79, v57
	v_pk_add_f32 v[82:83], v[82:83], 1.0 op_sel_hi:[1,0] neg_lo:[1,0] neg_hi:[1,0]
	v_mov_b32_e32 v84, v40
	v_mov_b32_e32 v85, v79
	v_mul_f32_e32 v79, 0xbfb8aa3b, v86
	v_pk_mul_f32 v[82:83], v[84:85], v[82:83]
	v_exp_f32_e32 v79, v79
	v_mul_f32_e32 v84, 0xbfb8aa3b, v87
	v_exp_f32_e32 v85, v84
	v_mul_f32_e32 v90, v96, v109
	v_add_f32_e32 v79, 1.0, v79
	v_rcp_f32_e32 v79, v79
	v_add_f32_e32 v85, 1.0, v85
	v_rcp_f32_e32 v96, v85
	v_mul_f32_e32 v91, v97, v49
	v_mul_f32_e32 v79, v79, v86
	v_mul_f32_e32 v93, v81, v61
	v_mov_b32_e32 v85, v81
	v_mul_f32_e32 v79, v90, v79
	v_mul_f32_e32 v81, v96, v87
	v_mul_f32_e32 v81, v91, v81
	v_cvt_pk_bf16_f32 v79, v79, v81
	v_mov_b32_e32 v66, v67
	v_mov_b32_e32 v67, v80
	ds_write_b32 v100, v79 offset:53728
	v_mul_f32_e32 v78, v78, v92
	v_mul_f32_e32 v79, v80, v93
	v_cvt_pk_bf16_f32 v80, v78, v79
	ds_read_b32 v81, v107
	v_pk_add_f32 v[66:67], v[66:67], 1.0 op_sel_hi:[1,0] neg_lo:[1,0] neg_hi:[1,0]
	v_mov_b32_e32 v84, v41
	v_pk_mul_f32 v[66:67], v[84:85], v[66:67]
	v_mul_f32_e32 v84, v54, v78
	v_mul_f32_e32 v85, v55, v79
	v_mov_b32_e32 v78, v62
	v_mov_b32_e32 v79, v82
	ds_write_b32 v100, v80 offset:32224
	s_waitcnt lgkmcnt(1)
	v_lshlrev_b32_e32 v86, 16, v81
	v_and_b32_e32 v87, 0xffff0000, v81
	v_pk_add_f32 v[78:79], v[78:79], 1.0 op_sel_hi:[1,0] neg_lo:[1,0] neg_hi:[1,0]
	v_mov_b32_e32 v80, v40
	v_mov_b32_e32 v81, v83
	v_pk_mul_f32 v[78:79], v[80:81], v[78:79]
	v_mul_f32_e32 v80, 0xbfb8aa3b, v86
	v_exp_f32_e32 v81, v80
	v_mul_f32_e32 v80, 0xbfb8aa3b, v87
	v_mul_f32_e32 v92, v83, v57
	v_exp_f32_e32 v83, v80
	v_add_f32_e32 v81, 1.0, v81
	v_mul_f32_e32 v90, v94, v109
	v_rcp_f32_e32 v94, v81
	v_add_f32_e32 v81, 1.0, v83
	v_rcp_f32_e32 v83, v81
	v_mul_f32_e32 v93, v67, v61
	v_mov_b32_e32 v81, v67
	v_mul_f32_e32 v67, v94, v86
	v_mul_f32_e32 v91, v95, v49
	v_mul_f32_e32 v67, v90, v67
	v_mul_f32_e32 v83, v83, v87
	v_mul_f32_e32 v83, v91, v83
	v_cvt_pk_bf16_f32 v67, v67, v83
	v_mov_b32_e32 v62, v63
	v_mov_b32_e32 v63, v66
	ds_write_b32 v100, v67 offset:53456
	v_mul_f32_e32 v67, v82, v92
	v_mul_f32_e32 v66, v66, v93
	v_cvt_pk_bf16_f32 v82, v67, v66
	ds_read_b32 v83, v106
	v_pk_add_f32 v[62:63], v[62:63], 1.0 op_sel_hi:[1,0] neg_lo:[1,0] neg_hi:[1,0]
	v_mov_b32_e32 v80, v41
	v_mul_f32_e32 v86, v64, v109
	v_mul_f32_e32 v87, v65, v49
	v_mov_b32_e32 v64, v52
	v_mov_b32_e32 v65, v78
	v_pk_mul_f32 v[62:63], v[80:81], v[62:63]
	ds_write_b32 v100, v82 offset:31952
	v_mul_f32_e32 v80, v54, v67
	v_mul_f32_e32 v81, v55, v66
	s_waitcnt lgkmcnt(1)
	v_lshlrev_b32_e32 v82, 16, v83
	v_pk_add_f32 v[64:65], v[64:65], 1.0 op_sel_hi:[1,0] neg_lo:[1,0] neg_hi:[1,0]
	v_mov_b32_e32 v66, v40
	v_mov_b32_e32 v67, v79
	v_and_b32_e32 v83, 0xffff0000, v83
	v_pk_mul_f32 v[64:65], v[66:67], v[64:65]
	v_mul_f32_e32 v66, 0xbfb8aa3b, v82
	v_exp_f32_e32 v67, v66
	v_mul_f32_e32 v66, 0xbfb8aa3b, v83
	v_mul_f32_e32 v90, v79, v57
	v_exp_f32_e32 v79, v66
	v_add_f32_e32 v67, 1.0, v67
	v_rcp_f32_e32 v92, v67
	v_mul_f32_e32 v91, v63, v61
	v_add_f32_e32 v67, 1.0, v79
	v_rcp_f32_e32 v79, v67
	v_mov_b32_e32 v67, v63
	v_mul_f32_e32 v63, v92, v82
	v_mul_f32_e32 v63, v86, v63
	v_mul_f32_e32 v79, v79, v83
	v_mul_f32_e32 v79, v87, v79
	v_cvt_pk_bf16_f32 v63, v63, v79
	v_mov_b32_e32 v52, v53
	v_mov_b32_e32 v53, v62
	ds_write_b32 v100, v63 offset:53184
	v_mul_f32_e32 v63, v78, v90
	v_mul_f32_e32 v62, v62, v91
	v_cvt_pk_bf16_f32 v78, v63, v62
	ds_read_b32 v77, v77
	v_mul_f32_e32 v83, v58, v109
	v_mul_f32_e32 v86, v59, v49
	v_mov_b32_e32 v58, v44
	v_mov_b32_e32 v59, v64
	ds_write_b32 v100, v78 offset:31680
	v_mul_f32_e32 v78, v54, v63
	v_mul_f32_e32 v79, v55, v62
	s_waitcnt lgkmcnt(1)
	v_lshlrev_b32_e32 v82, 16, v77
	v_pk_add_f32 v[58:59], v[58:59], 1.0 op_sel_hi:[1,0] neg_lo:[1,0] neg_hi:[1,0]
	v_mov_b32_e32 v62, v40
	v_mov_b32_e32 v63, v65
	v_and_b32_e32 v77, 0xffff0000, v77
	v_pk_mul_f32 v[58:59], v[62:63], v[58:59]
	v_mov_b32_e32 v62, v43
	v_mul_f32_e32 v43, 0xbfb8aa3b, v82
	v_exp_f32_e32 v43, v43
	v_mul_f32_e32 v44, 0xbfb8aa3b, v77
	v_exp_f32_e32 v44, v44
	v_pk_add_f32 v[52:53], v[52:53], 1.0 op_sel_hi:[1,0] neg_lo:[1,0] neg_hi:[1,0]
	v_add_f32_e32 v43, 1.0, v43
	v_rcp_f32_e32 v43, v43
	v_add_f32_e32 v44, 1.0, v44
	v_rcp_f32_e32 v44, v44
	v_mov_b32_e32 v66, v41
	v_mul_f32_e32 v43, v43, v82
	v_pk_mul_f32 v[52:53], v[66:67], v[52:53]
	v_mul_f32_e32 v43, v83, v43
	v_mul_f32_e32 v44, v44, v77
	v_mul_f32_e32 v87, v65, v57
	v_mul_f32_e32 v90, v53, v61
	v_mul_f32_e32 v44, v86, v44
	v_cvt_pk_bf16_f32 v43, v43, v44
	ds_write_b32 v100, v43 offset:52912
	v_mul_f32_e32 v43, v64, v87
	v_mul_f32_e32 v44, v52, v90
	v_cvt_pk_bf16_f32 v64, v43, v44
	ds_read_b32 v65, v76
	v_mov_b32_e32 v63, v52
	v_pk_add_f32 v[62:63], v[62:63], 1.0 op_sel_hi:[1,0] neg_lo:[1,0] neg_hi:[1,0]
	v_mov_b32_e32 v67, v53
	v_pk_mul_f32 v[52:53], v[66:67], v[62:63]
	ds_write_b32 v100, v64 offset:31408
	v_mul_f32_e32 v62, v54, v43
	s_waitcnt lgkmcnt(1)
	v_lshlrev_b32_e32 v64, 16, v65
	v_mov_b32_e32 v43, v58
	v_and_b32_e32 v65, 0xffff0000, v65
	v_mul_f32_e32 v66, v50, v109
	v_mul_f32_e32 v67, v51, v49
	v_pk_add_f32 v[42:43], v[42:43], 1.0 op_sel_hi:[1,0] neg_lo:[1,0] neg_hi:[1,0]
	v_mov_b32_e32 v50, v40
	v_mov_b32_e32 v51, v59
	v_mul_f32_e32 v40, 0xbfb8aa3b, v64
	v_pk_mul_f32 v[42:43], v[50:51], v[42:43]
	v_exp_f32_e32 v50, v40
	v_mul_f32_e32 v40, 0xbfb8aa3b, v65
	v_exp_f32_e32 v51, v40
	v_mov_b32_e32 v40, v41
	v_add_f32_e32 v41, 1.0, v50
	v_rcp_f32_e32 v50, v41
	v_add_f32_e32 v41, 1.0, v51
	v_rcp_f32_e32 v51, v41
	v_mul_f32_e32 v76, v59, v57
	v_mul_f32_e32 v50, v50, v64
	v_mul_f32_e32 v50, v66, v50
	v_mul_f32_e32 v51, v51, v65
	v_mul_f32_e32 v77, v53, v61
	v_mul_f32_e32 v51, v67, v51
	v_cvt_pk_bf16_f32 v50, v50, v51
	v_mul_f32_e32 v63, v55, v44
	v_mov_b32_e32 v44, v45
	v_mov_b32_e32 v45, v52
	v_mov_b32_e32 v41, v53
	ds_write_b32 v100, v50 offset:52640
	v_mul_f32_e32 v50, v58, v76
	v_mul_f32_e32 v51, v52, v77
	v_cvt_pk_bf16_f32 v52, v50, v51
	ds_read_b32 v53, v75
	v_pk_add_f32 v[44:45], v[44:45], 1.0 op_sel_hi:[1,0] neg_lo:[1,0] neg_hi:[1,0]
	v_mul_f32_e32 v47, v47, v49
	v_pk_mul_f32 v[40:41], v[40:41], v[44:45]
	v_mul_f32_e32 v44, v54, v50
	s_waitcnt lgkmcnt(0)
	v_lshlrev_b32_e32 v50, 16, v53
	v_mul_f32_e32 v45, v55, v51
	v_and_b32_e32 v51, 0xffff0000, v53
	v_mul_f32_e32 v49, 0xbfb8aa3b, v50
	ds_write_b32 v100, v52 offset:31136
	v_exp_f32_e32 v49, v49
	v_mul_f32_e32 v52, 0xbfb8aa3b, v51
	v_exp_f32_e32 v52, v52
	v_mul_f32_e32 v48, v48, v109
	v_add_f32_e32 v49, 1.0, v49
	v_rcp_f32_e32 v49, v49
	v_add_f32_e32 v52, 1.0, v52
	v_rcp_f32_e32 v52, v52
	v_mul_f32_e32 v43, v43, v57
	v_mul_f32_e32 v49, v49, v50
	v_mul_f32_e32 v48, v48, v49
	v_mul_f32_e32 v49, v52, v51
	v_mul_f32_e32 v47, v47, v49
	v_mul_f32_e32 v41, v41, v61
	v_cvt_pk_bf16_f32 v47, v48, v47
	v_add_u32_e32 v48, s46, v72
	ds_write_b32 v48, v47 offset:54272
	v_mul_f32_e32 v42, v42, v43
	v_mul_f32_e32 v40, v40, v41
	v_cvt_pk_bf16_f32 v41, v42, v40
	ds_write_b32 v48, v41 offset:32768
	v_mul_f32_e32 v41, v54, v42
	v_mul_f32_e32 v56, v54, v56
	v_mul_f32_e32 v47, v55, v40
	v_cvt_pk_bf16_f32 v40, v41, v44
	v_cvt_pk_bf16_f32 v41, v62, v78
	v_cvt_pk_bf16_f32 v42, v80, v84
	v_cvt_pk_bf16_f32 v43, v56, v88
	v_mul_f32_e32 v60, v55, v60
	ds_write_b128 v17, v[40:43]
	v_cvt_pk_bf16_f32 v40, v47, v45
	v_cvt_pk_bf16_f32 v41, v63, v79
	v_cvt_pk_bf16_f32 v42, v81, v85
	v_cvt_pk_bf16_f32 v43, v60, v89
	ds_write_b128 v17, v[40:43] offset:144
	s_cbranch_vccnz .LBB0_3018
	v_add_u32_e32 v40, 0x18400, v46
	ds_write_b64 v40, v[54:55]
